# stagedx
# baseline (speedup 1.0000x reference)
_Z10lstm_fusedPKfS0_S0_S0_S0_S0_S0_S0_S0_S0_S0_Pf:
	s_load_dwordx16 s[36:51], s[0:1], 0x0
	s_load_dwordx8 s[52:59], s[0:1], 0x40
	s_load_dword s21, s[0:1], 0x60
	v_readfirstlane_b32 s3, v0
	v_and_b32_e32 v69, 63, v0
	v_and_b32_e32 v68, 15, v0
	v_bfe_u32 v1, v0, 4, 2
	s_lshr_b32 s3, s3, 6
	s_mov_b32 s35, s3
	s_lshl_b32 s2, s2, 4
	s_add_i32 s20, s3, s2
	v_lshlrev_b32_e32 v2, 5, v1
	v_mov_b32_e32 v3, 0
	v_lshlrev_b32_e32 v60, 4, v0
	s_lshl_b32 s26, s20, 12
	s_waitcnt lgkmcnt(0)
	s_load_dword s34, s[56:57], 0x0
	v_lshl_add_u64 v[42:43], s[36:37], 0, v[2:3]
	v_lshl_or_b32 v2, v68, 7, s26
	v_lshl_add_u64 v[74:75], v[42:43], 0, v[2:3]
	s_add_u32 s4, s3, 0
	s_mov_b32 s24, 0
	s_mov_b32 s25, 0
	s_sub_u32 s5, s4, 12
	s_mov_b64 s[8:9], s[44:45]
	s_movk_i32 s10, 0x100
	s_movk_i32 s11, 16
	s_movk_i32 s12, 64
	s_mov_b32 s13, 0xbf2562dd
	s_mov_b32 s14, 0xbfa562dd
	s_mov_b32 s15, 1
	s_cmp_lt_u32 s4, 12
	s_cbranch_scc0 .Lpr0_cls
	s_lshl_b32 s5, s4, 1
	s_mov_b64 s[8:9], s[38:39]
	s_movk_i32 s10, 0x80
	s_movk_i32 s11, 32
	s_movk_i32 s12, 16
	s_mov_b32 s13, 0xbfb8aa3b
	s_mov_b32 s14, 0xc038aa3b

.Lpb_skip:
	s_cmp_lt_u32 s35, 4
	s_cbranch_scc0 .Lpx_skip
	global_load_dwordx4 v[10:13], v[74:75], off offset:16 nt
	global_load_dwordx4 v[14:17], v[74:75], off nt
	global_load_dwordx4 v[2:5], v[74:75], off offset:2064 nt
	global_load_dwordx4 v[6:9], v[74:75], off offset:2048 nt
.Lpx_skip:
	s_cmp_lt_u32 s35, 4
	s_cbranch_scc1 .Lpw_lead0
	s_waitcnt vmcnt(4)
	s_branch .Lpw_done0
.Lpw_lead0:
	s_waitcnt vmcnt(8)
.Lpw_done0:
	v_pk_mul_f32 v[18:19], v[18:19], v[48:49] op_sel_hi:[1,0]
	v_pk_mul_f32 v[20:21], v[20:21], v[48:49] op_sel_hi:[1,0]
	v_pk_mul_f32 v[22:23], v[22:23], v[48:49] op_sel_hi:[1,0]
	v_pk_mul_f32 v[24:25], v[24:25], v[48:49] op_sel_hi:[1,0]
	v_cvt_pk_f16_f32 v18, v18, v19
	v_cvt_pk_f16_f32 v19, v20, v21
	v_cvt_pk_f16_f32 v20, v22, v23
	v_cvt_pk_f16_f32 v21, v24, v25
	ds_write_b128 v60, v[18:21]
	s_cmp_lt_u32 s35, 4
	s_cbranch_scc1 .Lpw_lead1
	s_waitcnt vmcnt(2)
	s_branch .Lpw_done1
.Lpw_lead1:
	s_waitcnt vmcnt(6)
.Lpw_done1:
	v_pk_mul_f32 v[26:27], v[26:27], v[50:51] op_sel_hi:[1,0]
	v_pk_mul_f32 v[28:29], v[28:29], v[50:51] op_sel_hi:[1,0]
	v_pk_mul_f32 v[30:31], v[30:31], v[50:51] op_sel_hi:[1,0]
	v_pk_mul_f32 v[32:33], v[32:33], v[50:51] op_sel_hi:[1,0]
	v_cvt_pk_f16_f32 v26, v26, v27
	v_cvt_pk_f16_f32 v27, v28, v29
	v_cvt_pk_f16_f32 v28, v30, v31
	v_cvt_pk_f16_f32 v29, v32, v33
	ds_write_b128 v60, v[26:29] offset:16384
	s_cmp_lt_u32 s35, 4
	s_cbranch_scc1 .Lpw_lead2
	s_waitcnt vmcnt(0)
	s_branch .Lpw_done2
.Lpw_lead2:
	s_waitcnt vmcnt(4)
.Lpw_done2:
	v_pk_mul_f32 v[34:35], v[34:35], v[52:53] op_sel_hi:[1,0]
	v_pk_mul_f32 v[36:37], v[36:37], v[52:53] op_sel_hi:[1,0]
	v_pk_mul_f32 v[44:45], v[44:45], v[52:53] op_sel_hi:[1,0]
	v_pk_mul_f32 v[46:47], v[46:47], v[52:53] op_sel_hi:[1,0]
	v_cvt_pk_f16_f32 v34, v34, v35
	v_cvt_pk_f16_f32 v35, v36, v37
	v_cvt_pk_f16_f32 v36, v44, v45
	v_cvt_pk_f16_f32 v37, v46, v47
	s_cmp_eq_u32 s25, 1
	s_cbranch_scc1 .Lpr2_nowrite
	ds_write_b128 v60, v[34:37] offset:32768
.Lpr2_nowrite:
	s_movk_i32 s4, 0x1a0
	v_cmp_gt_u32_e32 vcc, s4, v0
	v_add_f32_e32 v50, v78, v79
	v_lshlrev_b32_e32 v18, 2, v0
	s_and_saveexec_b64 s[0:1], vcc
	v_fma_f32 v50, v76, v50, -v77
	ds_write_b32 v18, v50 offset:41984
	s_or_b64 exec, exec, s[0:1]
	s_mov_b64 s[14:15], s[58:59]
	s_waitcnt lgkmcnt(0)
	v_mov_b32_e32 v18, 0xbfb8aa3b
	s_lshl_b32 s3, s21, 4
	s_cmpk_gt_i32 s20, 0x7fff
	v_cmp_gt_u32_e32 vcc, 32, v69
	s_waitcnt lgkmcnt(0)
	v_mul_f32_e32 v18, s34, v18
	v_exp_f32_e32 v70, v18
	v_mov_b32_e32 v18, 0
	v_and_b32_e32 v71, 48, v0
	s_mov_b32 s10, s20
	s_barrier
	s_cbranch_scc1 .LBB0_37
	s_cmp_lt_u32 s35, 4
	s_cbranch_scc1 .Lpx_done
	global_load_dwordx4 v[10:13], v[74:75], off offset:16 nt
	global_load_dwordx4 v[14:17], v[74:75], off nt
	global_load_dwordx4 v[2:5], v[74:75], off offset:2064 nt
	global_load_dwordx4 v[6:9], v[74:75], off offset:2048 nt
.Lpx_done:
	s_sub_i32 s2, s20, s3
	s_add_i32 s9, s3, s20
	s_mov_b32 s4, 1.0
	s_mov_b32 s8, 0x3fb4c4be
	v_lshlrev_b32_e32 v72, 4, v69
	v_cmp_eq_u32_e64 s[0:1], 1, v1
	v_lshl_add_u32 v38, s2, 5, v69
	s_lshl_b32 s7, s21, 9
	v_mov_b32_e32 v18, 0
	s_mov_b32 s12, 0
	s_mov_b32 s2, 0x4a000000
	s_mov_b32 s5, s4
	s_mov_b32 s6, 0x3f34c4be
	v_mov_b64_e32 v[40:41], s[8:9]
	s_mov_b32 s8, 0x400a34e2
	s_mov_b32 s33, 0
	s_branch .LBB0_35
